# combine phase: non-temporal hint on the read-once loads (expert outputs, partials, residual)
# speedup vs baseline: 1.0103x; 1.0103x over previous
.LBB0_1681:
	v_mov_b32_e32 v2, 0x1a0000
	global_load_dword v2, v2, s[56:57] offset:1020
	v_mov_b32_e32 v99, 0
	v_lshlrev_b32_e32 v98, 4, v1
	v_lshl_add_u64 v[100:101], s[22:23], 0, v[98:99]
	v_lshl_add_u64 v[102:103], s[26:27], 0, v[98:99]
	v_lshrrev_b32_e32 v126, 5, v1
	v_or_b32_e32 v127, 2, v126
	v_or_b32_e32 v128, 4, v126
	v_or_b32_e32 v129, 6, v126
	s_movk_i32 s14, 0x1000
	s_waitcnt vmcnt(0)
	v_readfirstlane_b32 s2, v2
	s_min_i32 s3, s2, 0x88
	s_addk_i32 s3, 0xff7b
	s_cmp_lt_u32 s3, -5
	s_cselect_b32 s3, 4, 7
	s_cmpk_gt_i32 s2, 0x82
	s_cselect_b32 s12, s3, 14
	s_lshl_b32 s2, s24, 1
	s_ashr_i32 s3, s2, 31
	s_lshl_b64 s[2:3], s[2:3], 2
	s_add_u32 s2, s20, s2
	s_addc_u32 s3, s21, s3
	global_load_dwordx2 v[18:19], v99, s[2:3] nt
	s_ashr_i32 s25, s24, 31
	s_lshl_b64 s[2:3], s[24:25], 12
	s_add_u32 s2, s22, s2
	s_addc_u32 s3, s23, s3
	global_load_dwordx4 v[2:5], v98, s[2:3] nt
	s_waitcnt lgkmcnt(0)
	global_load_dwordx4 v[6:9], v98, s[2:3] offset:1024 nt
	global_load_dwordx4 v[10:13], v98, s[2:3] offset:2048 nt
	s_lshl_b32 s13, s12, 18
	s_waitcnt vmcnt(3)
	v_ashrrev_i32_e32 v15, 31, v18
	v_mov_b32_e32 v14, v18
	v_ashrrev_i32_e32 v17, 31, v19
	v_mov_b32_e32 v16, v19
	v_lshlrev_b64 v[14:15], 12, v[14:15]
	v_lshlrev_b64 v[16:17], 12, v[16:17]
	v_lshl_add_u64 v[14:15], s[26:27], 0, v[14:15]
	v_lshl_add_u64 v[16:17], s[26:27], 0, v[16:17]
	v_readfirstlane_b32 s4, v14
	v_readfirstlane_b32 s5, v15
	v_readfirstlane_b32 s6, v16
	v_readfirstlane_b32 s7, v17
	s_nop 2
	global_load_dwordx4 v[38:41], v98, s[4:5] offset:1024 nt
	global_load_dwordx4 v[34:37], v98, s[4:5] offset:2048 nt
	global_load_dwordx4 v[46:49], v98, s[6:7] offset:1024 nt
	global_load_dwordx4 v[42:45], v98, s[6:7] offset:2048 nt
	global_load_dwordx4 v[58:61], v98, s[4:5] offset:3072 nt
	global_load_dwordx4 v[50:53], v98, s[4:5] nt
	global_load_dwordx4 v[62:65], v98, s[6:7] offset:3072 nt
	global_load_dwordx4 v[54:57], v98, s[6:7] nt
	global_load_dwordx4 v[14:17], v98, s[2:3] offset:3072 nt
	v_readfirstlane_b32 s15, v18
	v_lshlrev_b32_e32 v98, 5, v1
	v_lshlrev_b32_e32 v18, 5, v0
	v_lshl_add_u64 v[104:105], s[54:55], 0, v[98:99]
	v_and_b32_e32 v98, 0x3e0, v18
	v_and_b32_e32 v0, 31, v0
	v_readfirstlane_b32 s16, v19
	v_lshl_add_u64 v[18:19], s[56:57], 0, v[98:99]
	s_mov_b64 s[4:5], 0x46b00000
	v_lshlrev_b32_e32 v98, 5, v0
	v_lshl_add_u64 v[106:107], v[18:19], 0, s[4:5]
	v_lshl_add_u64 v[0:1], s[56:57], 0, v[98:99]
	s_mov_b64 s[4:5], 0x46b00010
	s_mov_b32 s3, 0
	v_lshl_add_u64 v[0:1], v[0:1], 0, s[4:5]
	s_mov_b64 s[4:5], 0x40000
	v_mov_b32_e32 v98, 0x7fc00000
	s_branch .LBB0_1684

.LBB0_1687:
	s_lshl_b32 s6, s8, 1
	s_ashr_i32 s7, s6, 31
	s_lshl_b64 s[6:7], s[6:7], 2
	s_add_u32 s6, s20, s6
	s_addc_u32 s7, s21, s7
	global_load_dwordx2 v[108:109], v99, s[6:7] nt
	s_ashr_i32 s9, s8, 31
	s_lshl_b64 s[6:7], s[8:9], 12
	v_lshl_add_u64 v[110:111], v[100:101], 0, s[6:7]
	global_load_dwordx4 v[18:21], v[110:111], off nt
	global_load_dwordx4 v[22:25], v[110:111], off offset:1024 nt
	s_waitcnt vmcnt(2)
	v_ashrrev_i32_e32 v27, 31, v108
	v_mov_b32_e32 v26, v108
	v_ashrrev_i32_e32 v29, 31, v109
	v_mov_b32_e32 v28, v109
	v_lshlrev_b64 v[26:27], 12, v[26:27]
	v_lshlrev_b64 v[28:29], 12, v[28:29]
	v_lshl_add_u64 v[112:113], v[102:103], 0, v[26:27]
	v_lshl_add_u64 v[114:115], v[102:103], 0, v[28:29]
	global_load_dwordx4 v[82:85], v[112:113], off nt
	global_load_dwordx4 v[70:73], v[112:113], off offset:1024 nt
	global_load_dwordx4 v[86:89], v[114:115], off nt
	global_load_dwordx4 v[78:81], v[114:115], off offset:1024 nt
	global_load_dwordx4 v[66:69], v[112:113], off offset:2048 nt
	global_load_dwordx4 v[90:93], v[112:113], off offset:3072 nt
	global_load_dwordx4 v[74:77], v[114:115], off offset:2048 nt
	global_load_dwordx4 v[94:97], v[114:115], off offset:3072 nt
	global_load_dwordx4 v[30:33], v[110:111], off offset:2048 nt
	global_load_dwordx4 v[26:29], v[110:111], off offset:3072 nt
	v_readfirstlane_b32 s6, v108
	v_readfirstlane_b32 s7, v109
	s_cmp_lt_i32 s15, 0x8000
	s_cbranch_scc1 .LBB0_1686

.LBB0_1689:
	global_load_dwordx4 v[36:39], v[34:35], off nt
	global_load_dwordx4 v[108:111], v[34:35], off offset:16 nt
	s_add_i32 s2, s2, -1
	v_lshl_add_u64 v[34:35], v[34:35], 0, s[4:5]
	s_cmp_eq_u32 s2, 0
	s_waitcnt vmcnt(1)
	v_pk_add_f32 v[60:61], v[60:61], v[38:39]
	v_pk_add_f32 v[50:51], v[50:51], v[36:37]
	s_waitcnt vmcnt(0)
	v_pk_add_f32 v[58:59], v[58:59], v[110:111]
	v_pk_add_f32 v[52:53], v[52:53], v[108:109]
	s_cbranch_scc0 .LBB0_1689
	s_and_b32 s2, s15, 0xff
	s_lshl_b32 s2, s2, 10
	v_or_b32_e32 v36, s9, v127
	v_mov_b64_e32 v[34:35], s[2:3]
	v_mad_u64_u32 v[34:35], s[10:11], s13, v36, v[34:35]
	v_mov_b32_e32 v40, 0
	v_lshl_add_u64 v[34:35], v[0:1], 0, v[34:35]
	s_mov_b32 s10, s12
	v_mov_b32_e32 v41, v40
	v_mov_b32_e32 v108, v40
	v_mov_b32_e32 v109, v40
	v_mov_b32_e32 v38, v40
	v_mov_b32_e32 v39, v40
	v_mov_b32_e32 v110, v40
	v_mov_b32_e32 v111, v40
.LBB0_1691:
	global_load_dwordx4 v[112:115], v[34:35], off offset:-16 nt
	global_load_dwordx4 v[116:119], v[34:35], off nt
	s_add_i32 s10, s10, -1
	v_lshl_add_u64 v[34:35], v[34:35], 0, s[4:5]
	s_cmp_lg_u32 s10, 0
	s_waitcnt vmcnt(1)
	v_pk_add_f32 v[110:111], v[110:111], v[114:115]
	v_pk_add_f32 v[38:39], v[38:39], v[112:113]
	s_waitcnt vmcnt(0)
	v_pk_add_f32 v[108:109], v[108:109], v[118:119]
	v_pk_add_f32 v[40:41], v[40:41], v[116:117]
	s_cbranch_scc1 .LBB0_1691
	v_or_b32_e32 v36, s9, v128
	v_mov_b64_e32 v[34:35], s[2:3]
	v_mad_u64_u32 v[34:35], s[10:11], s13, v36, v[34:35]
	v_mov_b32_e32 v36, 0
	v_lshl_add_u64 v[116:117], v[0:1], 0, v[34:35]
	s_mov_b32 s10, s12
	v_mov_b32_e32 v37, v36
	v_mov_b32_e32 v112, v36
	v_mov_b32_e32 v113, v36
	v_mov_b32_e32 v34, v36
	v_mov_b32_e32 v35, v36
	v_mov_b32_e32 v114, v36
	v_mov_b32_e32 v115, v36
.LBB0_1693:
	global_load_dwordx4 v[118:121], v[116:117], off offset:-16 nt
	global_load_dwordx4 v[122:125], v[116:117], off nt
	s_add_i32 s10, s10, -1
	v_lshl_add_u64 v[116:117], v[116:117], 0, s[4:5]
	s_cmp_lg_u32 s10, 0
	s_waitcnt vmcnt(1)
	v_pk_add_f32 v[114:115], v[114:115], v[120:121]
	v_pk_add_f32 v[34:35], v[34:35], v[118:119]
	s_waitcnt vmcnt(0)
	v_pk_add_f32 v[112:113], v[112:113], v[124:125]
	v_pk_add_f32 v[36:37], v[36:37], v[122:123]
	s_cbranch_scc1 .LBB0_1693
	v_or_b32_e32 v118, s9, v129
	v_mov_b64_e32 v[116:117], s[2:3]
	v_mad_u64_u32 v[116:117], s[10:11], s13, v118, v[116:117]
	v_lshl_add_u64 v[124:125], v[0:1], 0, v[116:117]
	v_mov_b32_e32 v116, 0
	s_mov_b32 s2, s12
	v_mov_b32_e32 v117, v116
	v_mov_b32_e32 v118, v116
	v_mov_b32_e32 v119, v116
	v_mov_b32_e32 v120, v116
	v_mov_b32_e32 v121, v116
	v_mov_b32_e32 v122, v116
	v_mov_b32_e32 v123, v116
.LBB0_1695:
	global_load_dwordx4 v[130:133], v[124:125], off offset:-16 nt
	global_load_dwordx4 v[134:137], v[124:125], off nt
	s_add_i32 s2, s2, -1
	v_lshl_add_u64 v[124:125], v[124:125], 0, s[4:5]
	s_cmp_lg_u32 s2, 0
	s_waitcnt vmcnt(1)
	v_pk_add_f32 v[122:123], v[122:123], v[132:133]
	v_pk_add_f32 v[120:121], v[120:121], v[130:131]
	s_waitcnt vmcnt(0)
	v_pk_add_f32 v[118:119], v[118:119], v[136:137]
	v_pk_add_f32 v[116:117], v[116:117], v[134:135]
	s_cbranch_scc1 .LBB0_1695
	v_cvt_pk_bf16_f32 v34, v34, v35
	v_cvt_pk_bf16_f32 v35, v114, v115
	v_cvt_pk_bf16_f32 v36, v36, v37
	v_cvt_pk_bf16_f32 v37, v112, v113
	v_cvt_pk_bf16_f32 v38, v38, v39
	v_cvt_pk_bf16_f32 v39, v110, v111
	v_cvt_pk_bf16_f32 v40, v40, v41
	v_cvt_pk_bf16_f32 v41, v108, v109
	v_cvt_pk_bf16_f32 v50, v50, v51
	v_cvt_pk_bf16_f32 v51, v60, v61
	v_cvt_pk_bf16_f32 v52, v52, v53
	v_cvt_pk_bf16_f32 v53, v58, v59
	v_cvt_pk_bf16_f32 v58, v120, v121
	v_cvt_pk_bf16_f32 v59, v122, v123
	v_cvt_pk_bf16_f32 v60, v116, v117
	v_cvt_pk_bf16_f32 v61, v118, v119
	s_cmp_lt_i32 s16, 0x8000
	s_cbranch_scc1 .LBB0_1706

.LBB0_1698:
	global_load_dwordx4 v[44:47], v[42:43], off nt
	global_load_dwordx4 v[108:111], v[42:43], off offset:16 nt
	s_add_i32 s2, s2, -1
	v_lshl_add_u64 v[42:43], v[42:43], 0, s[4:5]
	s_cmp_eq_u32 s2, 0
	s_waitcnt vmcnt(1)
	v_pk_add_f32 v[64:65], v[64:65], v[46:47]
	v_pk_add_f32 v[54:55], v[54:55], v[44:45]
	s_waitcnt vmcnt(0)
	v_pk_add_f32 v[62:63], v[62:63], v[110:111]
	v_pk_add_f32 v[56:57], v[56:57], v[108:109]
	s_cbranch_scc0 .LBB0_1698
	s_and_b32 s2, s16, 0xff
	s_lshl_b32 s2, s2, 10
	v_or_b32_e32 v44, s9, v127
	v_mov_b64_e32 v[42:43], s[2:3]
	v_mad_u64_u32 v[42:43], s[10:11], s13, v44, v[42:43]
	v_mov_b32_e32 v48, 0
	v_lshl_add_u64 v[42:43], v[0:1], 0, v[42:43]
	s_mov_b32 s10, s12
	v_mov_b32_e32 v49, v48
	v_mov_b32_e32 v108, v48
	v_mov_b32_e32 v109, v48
	v_mov_b32_e32 v46, v48
	v_mov_b32_e32 v47, v48
	v_mov_b32_e32 v110, v48
	v_mov_b32_e32 v111, v48
.LBB0_1700:
	global_load_dwordx4 v[112:115], v[42:43], off offset:-16 nt
	global_load_dwordx4 v[116:119], v[42:43], off nt
	s_add_i32 s10, s10, -1
	v_lshl_add_u64 v[42:43], v[42:43], 0, s[4:5]
	s_cmp_lg_u32 s10, 0
	s_waitcnt vmcnt(1)
	v_pk_add_f32 v[110:111], v[110:111], v[114:115]
	v_pk_add_f32 v[46:47], v[46:47], v[112:113]
	s_waitcnt vmcnt(0)
	v_pk_add_f32 v[108:109], v[108:109], v[118:119]
	v_pk_add_f32 v[48:49], v[48:49], v[116:117]
	s_cbranch_scc1 .LBB0_1700
	v_or_b32_e32 v44, s9, v128
	v_mov_b64_e32 v[42:43], s[2:3]
	v_mad_u64_u32 v[42:43], s[10:11], s13, v44, v[42:43]
	v_mov_b32_e32 v44, 0
	v_lshl_add_u64 v[116:117], v[0:1], 0, v[42:43]
	s_mov_b32 s10, s12
	v_mov_b32_e32 v45, v44
	v_mov_b32_e32 v112, v44
	v_mov_b32_e32 v113, v44
	v_mov_b32_e32 v42, v44
	v_mov_b32_e32 v43, v44
	v_mov_b32_e32 v114, v44
	v_mov_b32_e32 v115, v44
.LBB0_1702:
	global_load_dwordx4 v[118:121], v[116:117], off offset:-16 nt
	global_load_dwordx4 v[122:125], v[116:117], off nt
	s_add_i32 s10, s10, -1
	v_lshl_add_u64 v[116:117], v[116:117], 0, s[4:5]
	s_cmp_lg_u32 s10, 0
	s_waitcnt vmcnt(1)
	v_pk_add_f32 v[114:115], v[114:115], v[120:121]
	v_pk_add_f32 v[42:43], v[42:43], v[118:119]
	s_waitcnt vmcnt(0)
	v_pk_add_f32 v[112:113], v[112:113], v[124:125]
	v_pk_add_f32 v[44:45], v[44:45], v[122:123]
	s_cbranch_scc1 .LBB0_1702
	v_or_b32_e32 v118, s9, v129
	v_mov_b64_e32 v[116:117], s[2:3]
	v_mad_u64_u32 v[116:117], s[10:11], s13, v118, v[116:117]
	v_lshl_add_u64 v[124:125], v[0:1], 0, v[116:117]
	v_mov_b32_e32 v116, 0
	s_mov_b32 s2, s12
	v_mov_b32_e32 v117, v116
	v_mov_b32_e32 v118, v116
	v_mov_b32_e32 v119, v116
	v_mov_b32_e32 v120, v116
	v_mov_b32_e32 v121, v116
	v_mov_b32_e32 v122, v116
	v_mov_b32_e32 v123, v116
.LBB0_1704:
	global_load_dwordx4 v[130:133], v[124:125], off offset:-16 nt
	global_load_dwordx4 v[134:137], v[124:125], off nt
	s_add_i32 s2, s2, -1
	v_lshl_add_u64 v[124:125], v[124:125], 0, s[4:5]
	s_cmp_lg_u32 s2, 0
	s_waitcnt vmcnt(1)
	v_pk_add_f32 v[122:123], v[122:123], v[132:133]
	v_pk_add_f32 v[120:121], v[120:121], v[130:131]
	s_waitcnt vmcnt(0)
	v_pk_add_f32 v[118:119], v[118:119], v[136:137]
	v_pk_add_f32 v[116:117], v[116:117], v[134:135]
	s_cbranch_scc1 .LBB0_1704
	v_cvt_pk_bf16_f32 v42, v42, v43
	v_cvt_pk_bf16_f32 v43, v114, v115
	v_cvt_pk_bf16_f32 v44, v44, v45
	v_cvt_pk_bf16_f32 v45, v112, v113
	v_cvt_pk_bf16_f32 v46, v46, v47
	v_cvt_pk_bf16_f32 v47, v110, v111
	v_cvt_pk_bf16_f32 v48, v48, v49
	v_cvt_pk_bf16_f32 v49, v108, v109
	v_cvt_pk_bf16_f32 v54, v54, v55
	v_cvt_pk_bf16_f32 v55, v64, v65
	v_cvt_pk_bf16_f32 v56, v56, v57
	v_cvt_pk_bf16_f32 v57, v62, v63
	v_cvt_pk_bf16_f32 v62, v120, v121
	v_cvt_pk_bf16_f32 v63, v122, v123
	v_cvt_pk_bf16_f32 v64, v116, v117
	v_cvt_pk_bf16_f32 v65, v118, v119

.LBB0_1710:
	s_lshl_b32 s16, s24, 1
	s_ashr_i32 s17, s16, 31
	s_lshl_b64 s[16:17], s[16:17], 2
	s_add_u32 s16, s20, s16
	s_addc_u32 s17, s21, s17
	global_load_dwordx2 v[108:109], v99, s[16:17] nt
	s_ashr_i32 s25, s24, 31
	s_lshl_b64 s[16:17], s[24:25], 12
	v_lshl_add_u64 v[110:111], v[100:101], 0, s[16:17]
	global_load_dwordx4 v[2:5], v[110:111], off nt
	global_load_dwordx4 v[6:9], v[110:111], off offset:1024 nt
	s_waitcnt vmcnt(2)
	v_ashrrev_i32_e32 v11, 31, v108
	v_mov_b32_e32 v10, v108
	v_ashrrev_i32_e32 v13, 31, v109
	v_mov_b32_e32 v12, v109
	v_lshlrev_b64 v[10:11], 12, v[10:11]
	v_lshlrev_b64 v[12:13], 12, v[12:13]
	v_lshl_add_u64 v[112:113], v[102:103], 0, v[10:11]
	v_lshl_add_u64 v[114:115], v[102:103], 0, v[12:13]
	global_load_dwordx4 v[50:53], v[112:113], off nt
	global_load_dwordx4 v[38:41], v[112:113], off offset:1024 nt
	global_load_dwordx4 v[54:57], v[114:115], off nt
	global_load_dwordx4 v[46:49], v[114:115], off offset:1024 nt
	global_load_dwordx4 v[34:37], v[112:113], off offset:2048 nt
	global_load_dwordx4 v[58:61], v[112:113], off offset:3072 nt
	global_load_dwordx4 v[42:45], v[114:115], off offset:2048 nt
	global_load_dwordx4 v[62:65], v[114:115], off offset:3072 nt
	global_load_dwordx4 v[10:13], v[110:111], off offset:2048 nt
	global_load_dwordx4 v[14:17], v[110:111], off offset:3072 nt
	v_readfirstlane_b32 s15, v108
	v_readfirstlane_b32 s16, v109
	s_cmp_lt_i32 s6, 0x8000
	s_cbranch_scc1 .LBB0_1709

.LBB0_1712:
	global_load_dwordx4 v[68:71], v[66:67], off nt
	global_load_dwordx4 v[108:111], v[66:67], off offset:16 nt
	s_add_i32 s2, s2, -1
	v_lshl_add_u64 v[66:67], v[66:67], 0, s[4:5]
	s_cmp_eq_u32 s2, 0
	s_waitcnt vmcnt(1)
	v_pk_add_f32 v[92:93], v[92:93], v[70:71]
	v_pk_add_f32 v[82:83], v[82:83], v[68:69]
	s_waitcnt vmcnt(0)
	v_pk_add_f32 v[90:91], v[90:91], v[110:111]
	v_pk_add_f32 v[84:85], v[84:85], v[108:109]
	s_cbranch_scc0 .LBB0_1712
	s_and_b32 s2, s6, 0xff
	s_lshl_b32 s2, s2, 10
	v_or_b32_e32 v68, s9, v127
	v_mov_b64_e32 v[66:67], s[2:3]
	v_mad_u64_u32 v[66:67], s[18:19], s13, v68, v[66:67]
	v_mov_b32_e32 v72, 0
	v_lshl_add_u64 v[66:67], v[0:1], 0, v[66:67]
	s_mov_b32 s17, s12
	v_mov_b32_e32 v73, v72
	v_mov_b32_e32 v108, v72
	v_mov_b32_e32 v109, v72
	v_mov_b32_e32 v70, v72
	v_mov_b32_e32 v71, v72
	v_mov_b32_e32 v110, v72
	v_mov_b32_e32 v111, v72
.LBB0_1714:
	global_load_dwordx4 v[112:115], v[66:67], off offset:-16 nt
	global_load_dwordx4 v[116:119], v[66:67], off nt
	s_add_i32 s17, s17, -1
	v_lshl_add_u64 v[66:67], v[66:67], 0, s[4:5]
	s_cmp_lg_u32 s17, 0
	s_waitcnt vmcnt(1)
	v_pk_add_f32 v[110:111], v[110:111], v[114:115]
	v_pk_add_f32 v[70:71], v[70:71], v[112:113]
	s_waitcnt vmcnt(0)
	v_pk_add_f32 v[108:109], v[108:109], v[118:119]
	v_pk_add_f32 v[72:73], v[72:73], v[116:117]
	s_cbranch_scc1 .LBB0_1714
	v_or_b32_e32 v68, s9, v128
	v_mov_b64_e32 v[66:67], s[2:3]
	v_mad_u64_u32 v[66:67], s[18:19], s13, v68, v[66:67]
	v_mov_b32_e32 v68, 0
	v_lshl_add_u64 v[116:117], v[0:1], 0, v[66:67]
	s_mov_b32 s17, s12
	v_mov_b32_e32 v69, v68
	v_mov_b32_e32 v112, v68
	v_mov_b32_e32 v113, v68
	v_mov_b32_e32 v66, v68
	v_mov_b32_e32 v67, v68
	v_mov_b32_e32 v114, v68
	v_mov_b32_e32 v115, v68
.LBB0_1716:
	global_load_dwordx4 v[118:121], v[116:117], off offset:-16 nt
	global_load_dwordx4 v[122:125], v[116:117], off nt
	s_add_i32 s17, s17, -1
	v_lshl_add_u64 v[116:117], v[116:117], 0, s[4:5]
	s_cmp_lg_u32 s17, 0
	s_waitcnt vmcnt(1)
	v_pk_add_f32 v[114:115], v[114:115], v[120:121]
	v_pk_add_f32 v[66:67], v[66:67], v[118:119]
	s_waitcnt vmcnt(0)
	v_pk_add_f32 v[112:113], v[112:113], v[124:125]
	v_pk_add_f32 v[68:69], v[68:69], v[122:123]
	s_cbranch_scc1 .LBB0_1716
	v_or_b32_e32 v118, s9, v129
	v_mov_b64_e32 v[116:117], s[2:3]
	v_mad_u64_u32 v[116:117], s[18:19], s13, v118, v[116:117]
	v_lshl_add_u64 v[124:125], v[0:1], 0, v[116:117]
	v_mov_b32_e32 v116, 0
	s_mov_b32 s2, s12
	v_mov_b32_e32 v117, v116
	v_mov_b32_e32 v118, v116
	v_mov_b32_e32 v119, v116
	v_mov_b32_e32 v120, v116
	v_mov_b32_e32 v121, v116
	v_mov_b32_e32 v122, v116
	v_mov_b32_e32 v123, v116
.LBB0_1718:
	global_load_dwordx4 v[130:133], v[124:125], off offset:-16 nt
	global_load_dwordx4 v[134:137], v[124:125], off nt
	s_add_i32 s2, s2, -1
	v_lshl_add_u64 v[124:125], v[124:125], 0, s[4:5]
	s_cmp_lg_u32 s2, 0
	s_waitcnt vmcnt(1)
	v_pk_add_f32 v[122:123], v[122:123], v[132:133]
	v_pk_add_f32 v[120:121], v[120:121], v[130:131]
	s_waitcnt vmcnt(0)
	v_pk_add_f32 v[118:119], v[118:119], v[136:137]
	v_pk_add_f32 v[116:117], v[116:117], v[134:135]
	s_cbranch_scc1 .LBB0_1718
	v_cvt_pk_bf16_f32 v66, v66, v67
	v_cvt_pk_bf16_f32 v67, v114, v115
	v_cvt_pk_bf16_f32 v68, v68, v69
	v_cvt_pk_bf16_f32 v69, v112, v113
	v_cvt_pk_bf16_f32 v70, v70, v71
	v_cvt_pk_bf16_f32 v71, v110, v111
	v_cvt_pk_bf16_f32 v72, v72, v73
	v_cvt_pk_bf16_f32 v73, v108, v109
	v_cvt_pk_bf16_f32 v82, v82, v83
	v_cvt_pk_bf16_f32 v83, v92, v93
	v_cvt_pk_bf16_f32 v84, v84, v85
	v_cvt_pk_bf16_f32 v85, v90, v91
	v_cvt_pk_bf16_f32 v90, v120, v121
	v_cvt_pk_bf16_f32 v91, v122, v123
	v_cvt_pk_bf16_f32 v92, v116, v117
	v_cvt_pk_bf16_f32 v93, v118, v119
	s_cmp_lt_i32 s7, 0x8000
	s_cbranch_scc1 .LBB0_1682

.LBB0_1721:
	global_load_dwordx4 v[76:79], v[74:75], off nt
	global_load_dwordx4 v[108:111], v[74:75], off offset:16 nt
	s_add_i32 s2, s2, -1
	v_lshl_add_u64 v[74:75], v[74:75], 0, s[4:5]
	s_cmp_eq_u32 s2, 0
	s_waitcnt vmcnt(1)
	v_pk_add_f32 v[96:97], v[96:97], v[78:79]
	v_pk_add_f32 v[86:87], v[86:87], v[76:77]
	s_waitcnt vmcnt(0)
	v_pk_add_f32 v[94:95], v[94:95], v[110:111]
	v_pk_add_f32 v[88:89], v[88:89], v[108:109]
	s_cbranch_scc0 .LBB0_1721
	s_and_b32 s2, s7, 0xff
	s_lshl_b32 s2, s2, 10
	v_or_b32_e32 v76, s9, v127
	v_mov_b64_e32 v[74:75], s[2:3]
	v_mad_u64_u32 v[74:75], s[18:19], s13, v76, v[74:75]
	v_mov_b32_e32 v80, 0
	v_lshl_add_u64 v[74:75], v[0:1], 0, v[74:75]
	s_mov_b32 s17, s12
	v_mov_b32_e32 v81, v80
	v_mov_b32_e32 v108, v80
	v_mov_b32_e32 v109, v80
	v_mov_b32_e32 v78, v80
	v_mov_b32_e32 v79, v80
	v_mov_b32_e32 v110, v80
	v_mov_b32_e32 v111, v80
.LBB0_1723:
	global_load_dwordx4 v[112:115], v[74:75], off offset:-16 nt
	global_load_dwordx4 v[116:119], v[74:75], off nt
	s_add_i32 s17, s17, -1
	v_lshl_add_u64 v[74:75], v[74:75], 0, s[4:5]
	s_cmp_lg_u32 s17, 0
	s_waitcnt vmcnt(1)
	v_pk_add_f32 v[110:111], v[110:111], v[114:115]
	v_pk_add_f32 v[78:79], v[78:79], v[112:113]
	s_waitcnt vmcnt(0)
	v_pk_add_f32 v[108:109], v[108:109], v[118:119]
	v_pk_add_f32 v[80:81], v[80:81], v[116:117]
	s_cbranch_scc1 .LBB0_1723
	v_or_b32_e32 v76, s9, v128
	v_mov_b64_e32 v[74:75], s[2:3]
	v_mad_u64_u32 v[74:75], s[18:19], s13, v76, v[74:75]
	v_mov_b32_e32 v76, 0
	v_lshl_add_u64 v[116:117], v[0:1], 0, v[74:75]
	s_mov_b32 s17, s12
	v_mov_b32_e32 v77, v76
	v_mov_b32_e32 v112, v76
	v_mov_b32_e32 v113, v76
	v_mov_b32_e32 v74, v76
	v_mov_b32_e32 v75, v76
	v_mov_b32_e32 v114, v76
	v_mov_b32_e32 v115, v76
.LBB0_1725:
	global_load_dwordx4 v[118:121], v[116:117], off offset:-16 nt
	global_load_dwordx4 v[122:125], v[116:117], off nt
	s_add_i32 s17, s17, -1
	v_lshl_add_u64 v[116:117], v[116:117], 0, s[4:5]
	s_cmp_lg_u32 s17, 0
	s_waitcnt vmcnt(1)
	v_pk_add_f32 v[114:115], v[114:115], v[120:121]
	v_pk_add_f32 v[74:75], v[74:75], v[118:119]
	s_waitcnt vmcnt(0)
	v_pk_add_f32 v[112:113], v[112:113], v[124:125]
	v_pk_add_f32 v[76:77], v[76:77], v[122:123]
	s_cbranch_scc1 .LBB0_1725
	v_or_b32_e32 v118, s9, v129
	v_mov_b64_e32 v[116:117], s[2:3]
	v_mad_u64_u32 v[116:117], s[18:19], s13, v118, v[116:117]
	v_lshl_add_u64 v[124:125], v[0:1], 0, v[116:117]
	v_mov_b32_e32 v116, 0
	s_mov_b32 s2, s12
	v_mov_b32_e32 v117, v116
	v_mov_b32_e32 v118, v116
	v_mov_b32_e32 v119, v116
	v_mov_b32_e32 v120, v116
	v_mov_b32_e32 v121, v116
	v_mov_b32_e32 v122, v116
	v_mov_b32_e32 v123, v116
.LBB0_1727:
	global_load_dwordx4 v[130:133], v[124:125], off offset:-16 nt
	global_load_dwordx4 v[134:137], v[124:125], off nt
	s_add_i32 s2, s2, -1
	v_lshl_add_u64 v[124:125], v[124:125], 0, s[4:5]
	s_cmp_lg_u32 s2, 0
	s_waitcnt vmcnt(1)
	v_pk_add_f32 v[122:123], v[122:123], v[132:133]
	v_pk_add_f32 v[120:121], v[120:121], v[130:131]
	s_waitcnt vmcnt(0)
	v_pk_add_f32 v[118:119], v[118:119], v[136:137]
	v_pk_add_f32 v[116:117], v[116:117], v[134:135]
	s_cbranch_scc1 .LBB0_1727
	v_cvt_pk_bf16_f32 v74, v74, v75
	v_cvt_pk_bf16_f32 v75, v114, v115
	v_cvt_pk_bf16_f32 v76, v76, v77
	v_cvt_pk_bf16_f32 v77, v112, v113
	v_cvt_pk_bf16_f32 v78, v78, v79
	v_cvt_pk_bf16_f32 v79, v110, v111
	v_cvt_pk_bf16_f32 v80, v80, v81
	v_cvt_pk_bf16_f32 v81, v108, v109
	v_cvt_pk_bf16_f32 v86, v86, v87
	v_cvt_pk_bf16_f32 v87, v96, v97
	v_cvt_pk_bf16_f32 v88, v88, v89
	v_cvt_pk_bf16_f32 v89, v94, v95
	v_cvt_pk_bf16_f32 v94, v120, v121
	v_cvt_pk_bf16_f32 v95, v122, v123
	v_cvt_pk_bf16_f32 v96, v116, v117
	v_cvt_pk_bf16_f32 v97, v118, v119
	s_branch .LBB0_1682
